# k_point: the Wq/Wk fp16 image staging (12 cvt+ds_write, exec-masked third stores) moved from behind the role code into the gelu phase (after 4 of 5 iterations) so the late role-1 waves reach barrier 2
# speedup vs baseline: 1.0146x; 1.0049x over previous
.LBB0_10:
	s_or_b64 exec, exec, s[8:9]
	s_waitcnt vmcnt(16)
	v_add_u32_e32 v70, v1, v107
	v_pk_add_f32 v[60:61], v[60:61], v[64:65]
	v_pk_add_f32 v[58:59], v[58:59], v[62:63]
	v_cvt_pk_f16_f32 v61, v60, v61
	v_cvt_pk_f16_f32 v60, v58, v59
	v_or_b32_e32 v58, v95, v70
	v_pk_add_f32 v[52:53], v[52:53], v[56:57]
	v_pk_add_f32 v[50:51], v[50:51], v[54:55]
	v_or_b32_e32 v1, v1, v102
	v_lshlrev_b32_e32 v71, 3, v102
	s_add_i32 s6, 0, 0x14300
	v_mul_u32_u24_e32 v58, 0x88, v58
	v_cvt_pk_f16_f32 v53, v52, v53
	v_cvt_pk_f16_f32 v52, v50, v51
	v_mul_u32_u24_e32 v1, 0x88, v1
	v_lshlrev_b32_e32 v50, 3, v95
	v_lshlrev_b32_e32 v93, 2, v95
	v_add3_u32 v58, s6, v71, v58
	v_add3_u32 v1, s6, v1, v50
	v_lshrrev_b32_e32 v50, 2, v102
	v_and_b32_e32 v87, 4, v93
	ds_write2_b64 v58, v[60:61], v[52:53] offset1:68
	v_or_b32_e32 v52, v87, v50
	v_or_b32_e32 v50, v93, v50
	s_movk_i32 s6, 0x2d00
	v_lshlrev_b32_e32 v95, 2, v102
	v_mul_u32_u24_e32 v50, 0x50, v50
	s_waitcnt lgkmcnt(0)
	s_barrier
	ds_read2_b64 v[54:57], v1 offset1:4
	ds_read2_b64 v[62:65], v1 offset0:8 offset1:12
	v_mad_u32_u24 v86, v104, s6, 0
	v_and_b32_e32 v51, 12, v95
	v_lshlrev_b32_e32 v88, 1, v50
	v_mul_u32_u24_e32 v91, 0x50, v52
	v_lshlrev_b32_e32 v92, 1, v51
	v_add_u32_e32 v121, v86, v88
	v_mul_u32_u24_e32 v1, 0x140, v104
	s_add_i32 s11, 0, 0x10e00
	v_lshl_add_u32 v96, v91, 1, v86
	v_add_u32_e32 v100, v121, v92
	v_cndmask_b32_e64 v122, 32, 16, s[4:5]
	v_cmp_gt_u32_e64 s[20:21], v122, v103
	s_waitcnt vmcnt(12)
	s_nop 1
	v_cndmask_b32_e64 v66, 0, v66, s[20:21]
	v_cndmask_b32_e64 v67, 0, v67, s[20:21]
	v_cndmask_b32_e64 v68, 0, v68, s[20:21]
	v_cndmask_b32_e64 v69, 0, v69, s[20:21]
	v_cvt_pk_f16_f32 v66, v66, v67
	v_cvt_pk_f16_f32 v67, v68, v69
	v_add3_u32 v1, s11, v1, v108
	v_add_u32_e32 v107, v96, v92
	v_add3_u32 v120, v86, v92, v88
	ds_read_b64_tr_b16 v[52:53], v100 offset:2560
	ds_read_b64_tr_b16 v[50:51], v120
	ds_read_b64_tr_b16 v[58:59], v120 offset:32
	ds_read_b64_tr_b16 v[68:69], v120 offset:5120
	ds_read_b64_tr_b16 v[70:71], v100 offset:7680
	ds_read_b128 v[72:75], v1
	ds_read_b128 v[76:79], v1 offset:64
	ds_read_b64_tr_b16 v[80:81], v120 offset:5152
	ds_read_b64_tr_b16 v[98:99], v120 offset:5248
	s_waitcnt vmcnt(15)
	ds_read_b64_tr_b16 v[108:109], v120 offset:64
	s_waitcnt vmcnt(12)
	ds_read_b64_tr_b16 v[112:113], v120 offset:5184
	s_waitcnt lgkmcnt(5)
	v_mfma_f32_16x16x32_f16 v[72:75], v[50:53], v[54:57], v[72:75]
	ds_read_b64_tr_b16 v[50:51], v107 offset:10240
	v_mov_b32_e32 v52, 0
	v_mov_b32_e32 v53, v52
	ds_read_b64_tr_b16 v[60:61], v100 offset:2592
	ds_read_b64_tr_b16 v[84:85], v100 offset:2688
	v_mfma_f32_16x16x32_f16 v[70:73], v[68:71], v[62:65], v[72:75]
	v_mov_b32_e32 v68, v52
	v_mov_b32_e32 v69, v52
	ds_read_b128 v[116:119], v1 offset:256
	s_waitcnt lgkmcnt(2)
	v_mfma_f32_16x16x32_f16 v[58:61], v[58:61], v[54:57], v[76:79]
	s_mov_b32 s7, 0x3fb504f3
	s_mov_b32 s9, 0x3ea7ba05
	s_mov_b32 s8, 0xbfba00e3
	v_mfma_f32_16x16x32_f16 v[70:73], v[50:53], v[66:69], v[70:73]
	ds_read_b64_tr_b16 v[82:83], v100 offset:7712
	ds_read_b64_tr_b16 v[110:111], v100 offset:2624
	ds_read_b64_tr_b16 v[50:51], v107 offset:10304
	v_mov_b32_e32 v76, v52
	v_mov_b32_e32 v77, v52
	s_waitcnt lgkmcnt(2)
	v_mfma_f32_16x16x32_f16 v[58:61], v[80:83], v[62:65], v[58:61]
	ds_read_b64_tr_b16 v[74:75], v107 offset:10272
	ds_read_b64_tr_b16 v[114:115], v100 offset:7744
	ds_read_b64_tr_b16 v[100:101], v100 offset:7808
	s_mov_b32 s6, 0x3f87dc22
	s_mov_b32 s10, 0xbe91a98e
	s_waitcnt lgkmcnt(2)
	v_mfma_f32_16x16x32_f16 v[74:77], v[74:77], v[66:69], v[58:61]
	s_nop 2
	ds_read_b128 v[58:61], v1 offset:128
	ds_read_b128 v[78:81], v1 offset:192
	v_or_b32_e32 v1, 48, v95
	v_lshlrev_b32_e32 v95, 1, v1
	v_add3_u32 v1, v86, v95, v88
	s_waitcnt lgkmcnt(1)
	v_mfma_f32_16x16x32_f16 v[58:61], v[108:111], v[54:57], v[58:61]
	ds_read_b64_tr_b16 v[108:109], v1
	ds_read_b64_tr_b16 v[82:83], v120 offset:128
	v_add_u32_e32 v120, v121, v95
	ds_read_b64_tr_b16 v[110:111], v120 offset:2560
	v_mfma_f32_16x16x32_f16 v[58:61], v[112:115], v[62:65], v[58:61]
	s_mov_b32 s12, 0x3e827906
	v_mfma_f32_16x16x32_f16 v[112:115], v[50:53], v[66:69], v[58:61]
	s_nop 5
	ds_read_b64_tr_b16 v[60:61], v120 offset:7680
	ds_read_b64_tr_b16 v[58:59], v1 offset:5120
	v_add_u32_e32 v1, v96, v95
	ds_read_b64_tr_b16 v[50:51], v1 offset:10240
	s_waitcnt lgkmcnt(3)
	v_mfma_f32_16x16x32_f16 v[78:81], v[108:111], v[54:57], v[78:81]
	s_waitcnt lgkmcnt(1)
	v_mfma_f32_16x16x32_f16 v[58:61], v[58:61], v[62:65], v[78:81]
	s_waitcnt lgkmcnt(0)
	v_mfma_f32_16x16x32_f16 v[58:61], v[50:53], v[66:69], v[58:61]
	ds_read_b64_tr_b16 v[50:51], v107 offset:10368
	v_mfma_f32_16x16x32_f16 v[54:57], v[82:85], v[54:57], v[116:119]
	v_mfma_f32_16x16x32_f16 v[54:57], v[98:101], v[62:65], v[54:57]
	s_waitcnt lgkmcnt(0)
	v_mfma_f32_16x16x32_f16 v[54:57], v[50:53], v[66:69], v[54:57]
	s_mov_b32 s24, 0x3fb504f3
	s_mov_b32 s26, 0x3ea7ba05
	s_mov_b32 s28, 0xbfb8aa3b
	s_mov_b32 s30, 0x3f87dc22
	s_mov_b32 s32, 0xbfba00e3
	s_mov_b32 s34, 0x3fb5f0e3
	s_mov_b32 s36, 0xbe91a98e
	s_mov_b32 s38, 0x3e827906
	v_mov_b32_e32 v152, s32
	v_mov_b32_e32 v153, s32
	v_pk_mul_f32 v[124:125], v[70:71], 0.5 op_sel_hi:[1,0]
	v_pk_mul_f32 v[138:139], v[72:73], 0.5 op_sel_hi:[1,0]
	v_and_b32_e32 v126, 0x7fffffff, v124
	v_and_b32_e32 v140, 0x7fffffff, v138
	v_and_b32_e32 v127, 0x7fffffff, v125
	v_and_b32_e32 v141, 0x7fffffff, v139
	v_pk_mul_f32 v[128:129], v[126:127], s[24:25] op_sel_hi:[1,0]
	v_pk_mul_f32 v[142:143], v[140:141], s[24:25] op_sel_hi:[1,0]
	v_pk_fma_f32 v[130:131], v[128:129], s[26:27], 1.0 op_sel_hi:[1,0,0]
	v_pk_fma_f32 v[144:145], v[142:143], s[26:27], 1.0 op_sel_hi:[1,0,0]
	v_pk_mul_f32 v[132:133], v[128:129], s[28:29] op_sel_hi:[1,0]
	v_pk_mul_f32 v[146:147], v[142:143], s[28:29] op_sel_hi:[1,0]
	v_rcp_f32_e32 v130, v130
	v_rcp_f32_e32 v144, v144
	v_rcp_f32_e32 v131, v131
	v_rcp_f32_e32 v145, v145
	v_pk_mul_f32 v[132:133], v[128:129], v[132:133]
	v_pk_mul_f32 v[146:147], v[142:143], v[146:147]
	v_exp_f32_e32 v132, v132
	v_exp_f32_e32 v146, v146
	v_exp_f32_e32 v133, v133
	v_exp_f32_e32 v147, v147
	v_pk_fma_f32 v[134:135], v[130:131], s[30:31], v[152:153] op_sel_hi:[1,0,0]
	v_pk_fma_f32 v[148:149], v[144:145], s[30:31], v[152:153] op_sel_hi:[1,0,0]
	v_pk_fma_f32 v[134:135], v[134:135], v[130:131], s[34:35] op_sel_hi:[1,1,0]
	v_pk_fma_f32 v[148:149], v[148:149], v[144:145], s[34:35] op_sel_hi:[1,1,0]
	v_pk_fma_f32 v[134:135], v[134:135], v[130:131], s[36:37] op_sel_hi:[1,1,0]
	v_pk_fma_f32 v[148:149], v[148:149], v[144:145], s[36:37] op_sel_hi:[1,1,0]
	v_pk_fma_f32 v[134:135], v[134:135], v[130:131], s[38:39] op_sel_hi:[1,1,0]
	v_pk_fma_f32 v[148:149], v[148:149], v[144:145], s[38:39] op_sel_hi:[1,1,0]
	v_pk_mul_f32 v[134:135], v[130:131], v[134:135]
	v_pk_mul_f32 v[148:149], v[144:145], v[148:149]
	v_pk_mul_f32 v[134:135], v[132:133], v[134:135]
	v_pk_mul_f32 v[148:149], v[146:147], v[148:149]
	v_pk_fma_f32 v[136:137], v[70:71], 0.5, v[126:127] op_sel_hi:[1,0,1]
	v_pk_fma_f32 v[150:151], v[72:73], 0.5, v[140:141] op_sel_hi:[1,0,1]
	v_pk_fma_f32 v[62:63], v[126:127], v[134:135], v[136:137] neg_lo:[1,0,0] neg_hi:[1,0,0]
	v_pk_fma_f32 v[64:65], v[140:141], v[148:149], v[150:151] neg_lo:[1,0,0] neg_hi:[1,0,0]
	v_pk_mul_f32 v[124:125], v[74:75], 0.5 op_sel_hi:[1,0]
	v_pk_mul_f32 v[138:139], v[76:77], 0.5 op_sel_hi:[1,0]
	v_and_b32_e32 v126, 0x7fffffff, v124
	v_and_b32_e32 v140, 0x7fffffff, v138
	v_and_b32_e32 v127, 0x7fffffff, v125
	v_and_b32_e32 v141, 0x7fffffff, v139
	v_pk_mul_f32 v[128:129], v[126:127], s[24:25] op_sel_hi:[1,0]
	v_pk_mul_f32 v[142:143], v[140:141], s[24:25] op_sel_hi:[1,0]
	v_pk_fma_f32 v[130:131], v[128:129], s[26:27], 1.0 op_sel_hi:[1,0,0]
	v_pk_fma_f32 v[144:145], v[142:143], s[26:27], 1.0 op_sel_hi:[1,0,0]
	v_pk_mul_f32 v[132:133], v[128:129], s[28:29] op_sel_hi:[1,0]
	v_pk_mul_f32 v[146:147], v[142:143], s[28:29] op_sel_hi:[1,0]
	v_rcp_f32_e32 v130, v130
	v_rcp_f32_e32 v144, v144
	v_rcp_f32_e32 v131, v131
	v_rcp_f32_e32 v145, v145
	v_pk_mul_f32 v[132:133], v[128:129], v[132:133]
	v_pk_mul_f32 v[146:147], v[142:143], v[146:147]
	v_exp_f32_e32 v132, v132
	v_exp_f32_e32 v146, v146
	v_exp_f32_e32 v133, v133
	v_exp_f32_e32 v147, v147
	v_pk_fma_f32 v[134:135], v[130:131], s[30:31], v[152:153] op_sel_hi:[1,0,0]
	v_pk_fma_f32 v[148:149], v[144:145], s[30:31], v[152:153] op_sel_hi:[1,0,0]
	v_pk_fma_f32 v[134:135], v[134:135], v[130:131], s[34:35] op_sel_hi:[1,1,0]
	v_pk_fma_f32 v[148:149], v[148:149], v[144:145], s[34:35] op_sel_hi:[1,1,0]
	v_pk_fma_f32 v[134:135], v[134:135], v[130:131], s[36:37] op_sel_hi:[1,1,0]
	v_pk_fma_f32 v[148:149], v[148:149], v[144:145], s[36:37] op_sel_hi:[1,1,0]
	v_pk_fma_f32 v[134:135], v[134:135], v[130:131], s[38:39] op_sel_hi:[1,1,0]
	v_pk_fma_f32 v[148:149], v[148:149], v[144:145], s[38:39] op_sel_hi:[1,1,0]
	v_pk_mul_f32 v[134:135], v[130:131], v[134:135]
	v_pk_mul_f32 v[148:149], v[144:145], v[148:149]
	v_pk_mul_f32 v[134:135], v[132:133], v[134:135]
	v_pk_mul_f32 v[148:149], v[146:147], v[148:149]
	v_pk_fma_f32 v[136:137], v[74:75], 0.5, v[126:127] op_sel_hi:[1,0,1]
	v_pk_fma_f32 v[150:151], v[76:77], 0.5, v[140:141] op_sel_hi:[1,0,1]
	v_pk_fma_f32 v[74:75], v[126:127], v[134:135], v[136:137] neg_lo:[1,0,0] neg_hi:[1,0,0]
	v_pk_fma_f32 v[76:77], v[140:141], v[148:149], v[150:151] neg_lo:[1,0,0] neg_hi:[1,0,0]
	v_pk_mul_f32 v[124:125], v[112:113], 0.5 op_sel_hi:[1,0]
	v_pk_mul_f32 v[138:139], v[114:115], 0.5 op_sel_hi:[1,0]
	v_and_b32_e32 v126, 0x7fffffff, v124
	v_and_b32_e32 v140, 0x7fffffff, v138
	v_and_b32_e32 v127, 0x7fffffff, v125
	v_and_b32_e32 v141, 0x7fffffff, v139
	v_pk_mul_f32 v[128:129], v[126:127], s[24:25] op_sel_hi:[1,0]
	v_pk_mul_f32 v[142:143], v[140:141], s[24:25] op_sel_hi:[1,0]
	v_pk_fma_f32 v[130:131], v[128:129], s[26:27], 1.0 op_sel_hi:[1,0,0]
	v_pk_fma_f32 v[144:145], v[142:143], s[26:27], 1.0 op_sel_hi:[1,0,0]
	v_pk_mul_f32 v[132:133], v[128:129], s[28:29] op_sel_hi:[1,0]
	v_pk_mul_f32 v[146:147], v[142:143], s[28:29] op_sel_hi:[1,0]
	v_rcp_f32_e32 v130, v130
	v_rcp_f32_e32 v144, v144
	v_rcp_f32_e32 v131, v131
	v_rcp_f32_e32 v145, v145
	v_pk_mul_f32 v[132:133], v[128:129], v[132:133]
	v_pk_mul_f32 v[146:147], v[142:143], v[146:147]
	v_exp_f32_e32 v132, v132
	v_exp_f32_e32 v146, v146
	v_exp_f32_e32 v133, v133
	v_exp_f32_e32 v147, v147
	v_pk_fma_f32 v[134:135], v[130:131], s[30:31], v[152:153] op_sel_hi:[1,0,0]
	v_pk_fma_f32 v[148:149], v[144:145], s[30:31], v[152:153] op_sel_hi:[1,0,0]
	v_pk_fma_f32 v[134:135], v[134:135], v[130:131], s[34:35] op_sel_hi:[1,1,0]
	v_pk_fma_f32 v[148:149], v[148:149], v[144:145], s[34:35] op_sel_hi:[1,1,0]
	v_pk_fma_f32 v[134:135], v[134:135], v[130:131], s[36:37] op_sel_hi:[1,1,0]
	v_pk_fma_f32 v[148:149], v[148:149], v[144:145], s[36:37] op_sel_hi:[1,1,0]
	v_pk_fma_f32 v[134:135], v[134:135], v[130:131], s[38:39] op_sel_hi:[1,1,0]
	v_pk_fma_f32 v[148:149], v[148:149], v[144:145], s[38:39] op_sel_hi:[1,1,0]
	v_pk_mul_f32 v[134:135], v[130:131], v[134:135]
	v_pk_mul_f32 v[148:149], v[144:145], v[148:149]
	v_pk_mul_f32 v[134:135], v[132:133], v[134:135]
	v_pk_mul_f32 v[148:149], v[146:147], v[148:149]
	v_pk_fma_f32 v[136:137], v[112:113], 0.5, v[126:127] op_sel_hi:[1,0,1]
	v_pk_fma_f32 v[150:151], v[114:115], 0.5, v[140:141] op_sel_hi:[1,0,1]
	v_pk_fma_f32 v[78:79], v[126:127], v[134:135], v[136:137] neg_lo:[1,0,0] neg_hi:[1,0,0]
	v_pk_fma_f32 v[80:81], v[140:141], v[148:149], v[150:151] neg_lo:[1,0,0] neg_hi:[1,0,0]
	v_pk_mul_f32 v[124:125], v[58:59], 0.5 op_sel_hi:[1,0]
	v_pk_mul_f32 v[138:139], v[60:61], 0.5 op_sel_hi:[1,0]
	v_and_b32_e32 v126, 0x7fffffff, v124
	v_and_b32_e32 v140, 0x7fffffff, v138
	v_and_b32_e32 v127, 0x7fffffff, v125
	v_and_b32_e32 v141, 0x7fffffff, v139
	v_pk_mul_f32 v[128:129], v[126:127], s[24:25] op_sel_hi:[1,0]
	v_pk_mul_f32 v[142:143], v[140:141], s[24:25] op_sel_hi:[1,0]
	v_pk_fma_f32 v[130:131], v[128:129], s[26:27], 1.0 op_sel_hi:[1,0,0]
	v_pk_fma_f32 v[144:145], v[142:143], s[26:27], 1.0 op_sel_hi:[1,0,0]
	v_pk_mul_f32 v[132:133], v[128:129], s[28:29] op_sel_hi:[1,0]
	v_pk_mul_f32 v[146:147], v[142:143], s[28:29] op_sel_hi:[1,0]
	v_rcp_f32_e32 v130, v130
	v_rcp_f32_e32 v144, v144
	v_rcp_f32_e32 v131, v131
	v_rcp_f32_e32 v145, v145
	v_pk_mul_f32 v[132:133], v[128:129], v[132:133]
	v_pk_mul_f32 v[146:147], v[142:143], v[146:147]
	v_exp_f32_e32 v132, v132
	v_exp_f32_e32 v146, v146
	v_exp_f32_e32 v133, v133
	v_exp_f32_e32 v147, v147
	v_pk_fma_f32 v[134:135], v[130:131], s[30:31], v[152:153] op_sel_hi:[1,0,0]
	v_pk_fma_f32 v[148:149], v[144:145], s[30:31], v[152:153] op_sel_hi:[1,0,0]
	v_pk_fma_f32 v[134:135], v[134:135], v[130:131], s[34:35] op_sel_hi:[1,1,0]
	v_pk_fma_f32 v[148:149], v[148:149], v[144:145], s[34:35] op_sel_hi:[1,1,0]
	v_pk_fma_f32 v[134:135], v[134:135], v[130:131], s[36:37] op_sel_hi:[1,1,0]
	v_pk_fma_f32 v[148:149], v[148:149], v[144:145], s[36:37] op_sel_hi:[1,1,0]
	v_pk_fma_f32 v[134:135], v[134:135], v[130:131], s[38:39] op_sel_hi:[1,1,0]
	v_pk_fma_f32 v[148:149], v[148:149], v[144:145], s[38:39] op_sel_hi:[1,1,0]
	v_pk_mul_f32 v[134:135], v[130:131], v[134:135]
	v_pk_mul_f32 v[148:149], v[144:145], v[148:149]
	v_pk_mul_f32 v[134:135], v[132:133], v[134:135]
	v_pk_mul_f32 v[148:149], v[146:147], v[148:149]
	v_pk_fma_f32 v[136:137], v[58:59], 0.5, v[126:127] op_sel_hi:[1,0,1]
	v_pk_fma_f32 v[150:151], v[60:61], 0.5, v[140:141] op_sel_hi:[1,0,1]
	v_pk_fma_f32 v[58:59], v[126:127], v[134:135], v[136:137] neg_lo:[1,0,0] neg_hi:[1,0,0]
	v_pk_fma_f32 v[60:61], v[140:141], v[148:149], v[150:151] neg_lo:[1,0,0] neg_hi:[1,0,0]
	s_waitcnt vmcnt(11)
	v_cvt_pk_f16_f32 v155, v48, v49
	v_cvt_pk_f16_f32 v154, v46, v47
	ds_write_b64 v90, v[154:155] offset:23040
	s_waitcnt vmcnt(10)
	v_cvt_pk_f16_f32 v155, v44, v45
	v_cvt_pk_f16_f32 v154, v42, v43
	ds_write_b64 v89, v[154:155] offset:23040
	s_and_saveexec_b64 s[22:23], s[2:3]
	s_cbranch_execz .LBB0_18
	v_mul_u32_u24_e32 v42, 0xe39, v106
	s_movk_i32 s6, 0xffee
	v_mul_i32_i24_sdwa v43, v42, s6 dst_sel:DWORD dst_unused:UNUSED_PAD src0_sel:WORD_1 src1_sel:DWORD
	s_movk_i32 s6, 0xa0
	s_waitcnt vmcnt(9)
	v_cvt_pk_f16_f32 v154, v38, v39
	v_mul_u32_u24_sdwa v38, v42, s6 dst_sel:DWORD dst_unused:UNUSED_PAD src0_sel:WORD_1 src1_sel:DWORD
	v_add_lshl_u32 v39, v43, v106, 3
	v_cvt_pk_f16_f32 v155, v40, v41
	v_add3_u32 v38, 0, v38, v39
	ds_write_b64 v38, v[154:155] offset:23040
.LBB0_18:
	s_or_b64 exec, exec, s[22:23]
	s_waitcnt vmcnt(8)
	v_cvt_pk_f16_f32 v155, v36, v37
	v_cvt_pk_f16_f32 v154, v34, v35
	ds_write_b64 v90, v[154:155] offset:34560
	s_waitcnt vmcnt(7)
	v_cvt_pk_f16_f32 v155, v32, v33
	v_cvt_pk_f16_f32 v154, v30, v31
	ds_write_b64 v89, v[154:155] offset:34560
	s_and_saveexec_b64 s[22:23], s[2:3]
	s_cbranch_execz .LBB0_20
	v_mul_u32_u24_e32 v30, 0xe39, v106
	s_movk_i32 s6, 0xffee
	v_mul_i32_i24_sdwa v31, v30, s6 dst_sel:DWORD dst_unused:UNUSED_PAD src0_sel:WORD_1 src1_sel:DWORD
	s_movk_i32 s6, 0xa0
	s_waitcnt vmcnt(6)
	v_cvt_pk_f16_f32 v154, v26, v27
	v_mul_u32_u24_sdwa v26, v30, s6 dst_sel:DWORD dst_unused:UNUSED_PAD src0_sel:WORD_1 src1_sel:DWORD
	v_add_lshl_u32 v27, v31, v106, 3
	v_cvt_pk_f16_f32 v155, v28, v29
	v_add3_u32 v26, 0, v26, v27
	ds_write_b64 v26, v[154:155] offset:34560
.LBB0_20:
	s_or_b64 exec, exec, s[22:23]
	s_waitcnt vmcnt(5)
	v_cvt_pk_f16_f32 v155, v24, v25
	v_cvt_pk_f16_f32 v154, v22, v23
	v_lshlrev_b32_e32 v135, 3, v106
	ds_write_b64 v135, v[154:155] offset:37888
	s_waitcnt vmcnt(4)
	v_cvt_pk_f16_f32 v155, v20, v21
	v_cvt_pk_f16_f32 v154, v18, v19
	ds_write_b64 v135, v[154:155] offset:41984
	s_and_saveexec_b64 s[22:23], s[2:3]
	s_cbranch_execz .LBB0_22
	v_mul_u32_u24_e32 v18, 0xe39, v106
	s_movk_i32 s6, 0xffee
	v_mul_i32_i24_sdwa v19, v18, s6 dst_sel:DWORD dst_unused:UNUSED_PAD src0_sel:WORD_1 src1_sel:DWORD
	s_movk_i32 s6, 0xa0
	s_waitcnt vmcnt(3)
	v_cvt_pk_f16_f32 v154, v14, v15
	v_mul_u32_u24_sdwa v14, v18, s6 dst_sel:DWORD dst_unused:UNUSED_PAD src0_sel:WORD_1 src1_sel:DWORD
	v_add_lshl_u32 v15, v19, v106, 3
	v_cvt_pk_f16_f32 v155, v16, v17
	v_add3_u32 v14, 0, v14, v15
	ds_write_b64 v135, v[154:155] offset:46080
.LBB0_22:
	s_or_b64 exec, exec, s[22:23]
	s_waitcnt vmcnt(2)
	v_cvt_pk_f16_f32 v155, v12, v13
	v_cvt_pk_f16_f32 v154, v10, v11
	ds_write_b64 v135, v[154:155] offset:49408
	s_waitcnt vmcnt(1)
	v_cvt_pk_f16_f32 v155, v8, v9
	v_cvt_pk_f16_f32 v154, v6, v7
	ds_write_b64 v135, v[154:155] offset:53504
	s_and_saveexec_b64 s[0:1], s[2:3]
	s_cbranch_execz .LBB0_24
	v_mul_u32_u24_e32 v6, 0xe39, v106
	s_movk_i32 s2, 0xffee
	v_mul_i32_i24_sdwa v7, v6, s2 dst_sel:DWORD dst_unused:UNUSED_PAD src0_sel:WORD_1 src1_sel:DWORD
	s_movk_i32 s2, 0xa0
	s_waitcnt vmcnt(0)
	v_cvt_pk_f16_f32 v154, v2, v3
	v_mul_u32_u24_sdwa v2, v6, s2 dst_sel:DWORD dst_unused:UNUSED_PAD src0_sel:WORD_1 src1_sel:DWORD
	v_add_lshl_u32 v3, v7, v106, 3
	v_cvt_pk_f16_f32 v155, v4, v5
	v_add3_u32 v2, 0, v2, v3
	ds_write_b64 v135, v[154:155] offset:57600
.LBB0_24:
	s_or_b64 exec, exec, s[0:1]
	s_waitcnt vmcnt(0)
	v_pk_mul_f32 v[124:125], v[54:55], 0.5 op_sel_hi:[1,0]
	v_pk_mul_f32 v[138:139], v[56:57], 0.5 op_sel_hi:[1,0]
	v_and_b32_e32 v126, 0x7fffffff, v124
	v_and_b32_e32 v140, 0x7fffffff, v138
	v_and_b32_e32 v127, 0x7fffffff, v125
	v_and_b32_e32 v141, 0x7fffffff, v139
	v_pk_mul_f32 v[128:129], v[126:127], s[24:25] op_sel_hi:[1,0]
	v_pk_mul_f32 v[142:143], v[140:141], s[24:25] op_sel_hi:[1,0]
	v_pk_fma_f32 v[130:131], v[128:129], s[26:27], 1.0 op_sel_hi:[1,0,0]
	v_pk_fma_f32 v[144:145], v[142:143], s[26:27], 1.0 op_sel_hi:[1,0,0]
	v_pk_mul_f32 v[132:133], v[128:129], s[28:29] op_sel_hi:[1,0]
	v_pk_mul_f32 v[146:147], v[142:143], s[28:29] op_sel_hi:[1,0]
	v_rcp_f32_e32 v130, v130
	v_rcp_f32_e32 v144, v144
	v_rcp_f32_e32 v131, v131
	v_rcp_f32_e32 v145, v145
	v_pk_mul_f32 v[132:133], v[128:129], v[132:133]
	v_pk_mul_f32 v[146:147], v[142:143], v[146:147]
	v_exp_f32_e32 v132, v132
	v_exp_f32_e32 v146, v146
	v_exp_f32_e32 v133, v133
	v_exp_f32_e32 v147, v147
	v_pk_fma_f32 v[134:135], v[130:131], s[30:31], v[152:153] op_sel_hi:[1,0,0]
	v_pk_fma_f32 v[148:149], v[144:145], s[30:31], v[152:153] op_sel_hi:[1,0,0]
	v_pk_fma_f32 v[134:135], v[134:135], v[130:131], s[34:35] op_sel_hi:[1,1,0]
	v_pk_fma_f32 v[148:149], v[148:149], v[144:145], s[34:35] op_sel_hi:[1,1,0]
	v_pk_fma_f32 v[134:135], v[134:135], v[130:131], s[36:37] op_sel_hi:[1,1,0]
	v_pk_fma_f32 v[148:149], v[148:149], v[144:145], s[36:37] op_sel_hi:[1,1,0]
	v_pk_fma_f32 v[134:135], v[134:135], v[130:131], s[38:39] op_sel_hi:[1,1,0]
	v_pk_fma_f32 v[148:149], v[148:149], v[144:145], s[38:39] op_sel_hi:[1,1,0]
	v_pk_mul_f32 v[134:135], v[130:131], v[134:135]
	v_pk_mul_f32 v[148:149], v[144:145], v[148:149]
	v_pk_mul_f32 v[134:135], v[132:133], v[134:135]
	v_pk_mul_f32 v[148:149], v[146:147], v[148:149]
	v_pk_fma_f32 v[136:137], v[54:55], 0.5, v[126:127] op_sel_hi:[1,0,1]
	v_pk_fma_f32 v[150:151], v[56:57], 0.5, v[140:141] op_sel_hi:[1,0,1]
	v_pk_fma_f32 v[82:83], v[126:127], v[134:135], v[136:137] neg_lo:[1,0,0] neg_hi:[1,0,0]
	v_pk_fma_f32 v[84:85], v[140:141], v[148:149], v[150:151] neg_lo:[1,0,0] neg_hi:[1,0,0]
	v_cvt_pk_f16_f32 v73, v60, v61
	v_cvt_pk_f16_f32 v71, v80, v81
	v_cvt_pk_f16_f32 v70, v78, v79
	v_cvt_pk_f16_f32 v72, v58, v59
	v_cvt_pk_f16_f32 v69, v76, v77
	v_lshlrev_b32_e32 v50, 1, v93
	v_cvt_pk_f16_f32 v67, v64, v65
	v_cvt_pk_f16_f32 v66, v62, v63
	v_cvt_pk_f16_f32 v68, v74, v75
	s_and_saveexec_b64 s[6:7], s[4:5]
	s_xor_b64 s[6:7], exec, s[6:7]
	s_cbranch_execz .LBB0_14
	s_movk_i32 s10, 0x48
	v_mul_lo_u32 v0, v97, s10
	v_ashrrev_i32_e32 v1, 31, v0
	v_mov_b32_e32 v51, v52
	s_waitcnt lgkmcnt(0)
	v_lshl_add_u64 v[0:1], v[0:1], 1, s[64:65]
	v_lshl_add_u64 v[0:1], v[0:1], 0, v[50:51]
	v_cvt_pk_f16_f32 v55, v64, v65
	v_cvt_pk_f16_f32 v54, v62, v63
	global_store_dwordx2 v[0:1], v[54:55], off
	v_cvt_pk_f16_f32 v55, v76, v77
	v_cvt_pk_f16_f32 v54, v74, v75
	global_store_dwordx2 v[0:1], v[54:55], off offset:32
	v_cvt_pk_f16_f32 v55, v80, v81
	v_cvt_pk_f16_f32 v54, v78, v79
	v_cmp_gt_u32_e64 s[4:5], 32, v103
	global_store_dwordx2 v[0:1], v[54:55], off offset:64
	v_cvt_pk_f16_f32 v55, v60, v61
	v_cvt_pk_f16_f32 v54, v58, v59
	global_store_dwordx2 v[0:1], v[54:55], off offset:96
	s_and_saveexec_b64 s[8:9], s[4:5]
	s_cbranch_execz .LBB0_13
	v_cvt_pk_f16_f32 v55, v84, v85
	v_cvt_pk_f16_f32 v54, v82, v83
	global_store_dwordx2 v[0:1], v[54:55], off offset:128

.LBB0_16:
	s_or_b64 exec, exec, s[6:7]
	v_cmp_ne_u32_e64 s[0:1], 0, v104
	s_waitcnt lgkmcnt(0)
	s_barrier
	s_and_saveexec_b64 s[2:3], s[0:1]
	s_cbranch_execz .LBB0_26
	s_add_i32 s0, 0, 0x11300
	v_mul_u32_u24_e32 v0, 0xc00, v105
	v_add3_u32 v0, s0, v94, v0
	ds_read_b128 v[62:65], v0
	ds_read_b128 v[58:61], v0 offset:1024
	ds_read_b128 v[54:57], v0 offset:2048
	s_waitcnt lgkmcnt(2)
	v_mov_b32_e32 v52, v62
